# final combine loop: the 28 loads of column chunks 1..7 of a row issued right after chunk 0's loads into free VGPRs, counted waits, instead of one load group per chunk behind the previous chunk's store
# speedup vs baseline: 1.0039x; 1.0039x over previous
.LBB0_2785:
	s_ashr_i32 s7, s6, 31
	s_lshl_b64 s[10:11], s[6:7], 2
	s_add_u32 s20, s14, s10
	s_addc_u32 s21, s15, s11
	global_load_dwordx2 v[10:11], v[4:5], off
	global_load_dwordx2 v[12:13], v1, s[20:21]
	s_add_i32 s22, s6, 1
	s_ashr_i32 s23, s22, 31
	s_add_u32 s10, s16, s10
	s_addc_u32 s11, s17, s11
	global_load_dword v0, v1, s[10:11]
	s_lshl_b64 s[20:21], s[22:23], 2
	s_add_u32 s10, s16, s20
	s_addc_u32 s11, s17, s21
	s_ashr_i32 s1, s0, 11
	s_mul_hi_i32 s3, s1, 0xc000
	s_mul_i32 s1, s1, 0xc000
	global_load_dword v8, v1, s[10:11]
	s_add_u32 s10, s12, s1
	s_addc_u32 s11, s13, s3
	global_load_dwordx4 v[18:21], v9, s[10:11]
	s_add_i32 s0, s0, s2
	s_add_i32 s6, s6, s18
	s_cmp_lt_i32 s0, 0x8000
	s_waitcnt vmcnt(4)
	v_lshlrev_b32_e32 v22, 16, v10
	v_and_b32_e32 v23, 0xffff0000, v10
	v_lshlrev_b32_e32 v24, 16, v11
	v_and_b32_e32 v25, 0xffff0000, v11
	s_waitcnt vmcnt(3)
	v_ashrrev_i32_e32 v11, 31, v12
	v_mov_b32_e32 v10, v12
	v_ashrrev_i32_e32 v27, 31, v13
	v_mov_b32_e32 v26, v13
	v_lshlrev_b64 v[10:11], 12, v[10:11]
	v_lshlrev_b64 v[12:13], 12, v[26:27]
	v_lshl_add_u64 v[10:11], v[2:3], 0, v[10:11]
	v_lshl_add_u64 v[12:13], v[2:3], 0, v[12:13]
	global_load_dwordx2 v[26:27], v[10:11], off
	global_load_dwordx2 v[28:29], v[12:13], off
	global_load_dwordx2 v[34:35], v[4:5], off offset:512
	global_load_dwordx2 v[36:37], v[10:11], off offset:512
	global_load_dwordx2 v[38:39], v[12:13], off offset:512
	global_load_dwordx4 v[40:43], v9, s[10:11] offset:1024
	global_load_dwordx2 v[44:45], v[4:5], off offset:1024
	global_load_dwordx2 v[46:47], v[10:11], off offset:1024
	global_load_dwordx2 v[48:49], v[12:13], off offset:1024
	global_load_dwordx4 v[50:53], v9, s[10:11] offset:2048
	global_load_dwordx2 v[54:55], v[4:5], off offset:1536
	global_load_dwordx2 v[56:57], v[10:11], off offset:1536
	global_load_dwordx2 v[58:59], v[12:13], off offset:1536
	global_load_dwordx4 v[60:63], v9, s[10:11] offset:3072
	global_load_dwordx2 v[64:65], v[4:5], off offset:2048
	global_load_dwordx2 v[66:67], v[10:11], off offset:2048
	global_load_dwordx2 v[68:69], v[12:13], off offset:2048
	global_load_dwordx4 v[70:73], v14, s[10:11]
	global_load_dwordx2 v[74:75], v[4:5], off offset:2560
	global_load_dwordx2 v[76:77], v[10:11], off offset:2560
	global_load_dwordx2 v[78:79], v[12:13], off offset:2560
	global_load_dwordx4 v[80:83], v15, s[10:11]
	global_load_dwordx2 v[84:85], v[4:5], off offset:3072
	global_load_dwordx2 v[86:87], v[10:11], off offset:3072
	global_load_dwordx2 v[88:89], v[12:13], off offset:3072
	global_load_dwordx4 v[90:93], v16, s[10:11]
	global_load_dwordx2 v[94:95], v[4:5], off offset:3584
	global_load_dwordx2 v[96:97], v[10:11], off offset:3584
	global_load_dwordx2 v[98:99], v[12:13], off offset:3584
	global_load_dwordx4 v[100:103], v17, s[10:11]
	s_waitcnt vmcnt(29)
	v_lshlrev_b32_e32 v30, 16, v26
	s_waitcnt vmcnt(28)
	v_lshlrev_b32_e32 v32, 16, v28
	v_and_b32_e32 v33, 0xffff0000, v28
	v_lshlrev_b32_e32 v28, 16, v29
	v_and_b32_e32 v29, 0xffff0000, v29
	v_and_b32_e32 v31, 0xffff0000, v26
	v_lshlrev_b32_e32 v26, 16, v27
	v_and_b32_e32 v27, 0xffff0000, v27
	v_pk_mul_f32 v[32:33], v[8:9], v[32:33] op_sel_hi:[0,1]
	v_pk_mul_f32 v[28:29], v[8:9], v[28:29] op_sel_hi:[0,1]
	v_pk_fma_f32 v[30:31], v[0:1], v[30:31], v[32:33] op_sel_hi:[0,1,1]
	v_pk_fma_f32 v[26:27], v[0:1], v[26:27], v[28:29] op_sel_hi:[0,1,1]
	v_pk_fma_f32 v[18:19], v[18:19], v[30:31], v[22:23]
	v_pk_fma_f32 v[20:21], v[20:21], v[26:27], v[24:25]
	global_store_dwordx4 v[6:7], v[18:21], off offset:-4096
	s_nop 0
	s_nop 0
	s_nop 0
	s_nop 0
	s_nop 0
	s_waitcnt vmcnt(25)
	v_mov_b32_e32 v22, v34
	v_mov_b32_e32 v23, v35
	v_mov_b32_e32 v24, v36
	v_mov_b32_e32 v25, v37
	v_mov_b32_e32 v26, v38
	v_mov_b32_e32 v27, v39
	v_mov_b32_e32 v18, v40
	v_mov_b32_e32 v19, v41
	v_mov_b32_e32 v20, v42
	v_mov_b32_e32 v21, v43
	v_lshlrev_b32_e32 v28, 16, v22
	s_nop 0
	v_lshlrev_b32_e32 v30, 16, v24
	s_nop 0
	v_lshlrev_b32_e32 v32, 16, v26
	v_and_b32_e32 v33, 0xffff0000, v26
	v_lshlrev_b32_e32 v26, 16, v27
	v_and_b32_e32 v27, 0xffff0000, v27
	v_and_b32_e32 v31, 0xffff0000, v24
	v_lshlrev_b32_e32 v24, 16, v25
	v_and_b32_e32 v25, 0xffff0000, v25
	v_pk_mul_f32 v[32:33], v[8:9], v[32:33] op_sel_hi:[0,1]
	v_pk_mul_f32 v[26:27], v[8:9], v[26:27] op_sel_hi:[0,1]
	v_and_b32_e32 v29, 0xffff0000, v22
	v_lshlrev_b32_e32 v22, 16, v23
	v_and_b32_e32 v23, 0xffff0000, v23
	v_pk_fma_f32 v[30:31], v[0:1], v[30:31], v[32:33] op_sel_hi:[0,1,1]
	v_pk_fma_f32 v[24:25], v[0:1], v[24:25], v[26:27] op_sel_hi:[0,1,1]
	s_nop 0
	v_pk_fma_f32 v[18:19], v[18:19], v[30:31], v[28:29]
	v_pk_fma_f32 v[20:21], v[20:21], v[24:25], v[22:23]
	global_store_dwordx4 v[6:7], v[18:21], off offset:-3072
	s_nop 0
	s_nop 0
	s_nop 0
	s_nop 0
	s_nop 0
	s_waitcnt vmcnt(22)
	v_mov_b32_e32 v22, v44
	v_mov_b32_e32 v23, v45
	v_mov_b32_e32 v24, v46
	v_mov_b32_e32 v25, v47
	v_mov_b32_e32 v26, v48
	v_mov_b32_e32 v27, v49
	v_mov_b32_e32 v18, v50
	v_mov_b32_e32 v19, v51
	v_mov_b32_e32 v20, v52
	v_mov_b32_e32 v21, v53
	v_lshlrev_b32_e32 v28, 16, v22
	s_nop 0
	v_lshlrev_b32_e32 v30, 16, v24
	s_nop 0
	v_lshlrev_b32_e32 v32, 16, v26
	v_and_b32_e32 v33, 0xffff0000, v26
	v_lshlrev_b32_e32 v26, 16, v27
	v_and_b32_e32 v27, 0xffff0000, v27
	v_and_b32_e32 v31, 0xffff0000, v24
	v_lshlrev_b32_e32 v24, 16, v25
	v_and_b32_e32 v25, 0xffff0000, v25
	v_pk_mul_f32 v[32:33], v[8:9], v[32:33] op_sel_hi:[0,1]
	v_pk_mul_f32 v[26:27], v[8:9], v[26:27] op_sel_hi:[0,1]
	v_and_b32_e32 v29, 0xffff0000, v22
	v_lshlrev_b32_e32 v22, 16, v23
	v_and_b32_e32 v23, 0xffff0000, v23
	v_pk_fma_f32 v[30:31], v[0:1], v[30:31], v[32:33] op_sel_hi:[0,1,1]
	v_pk_fma_f32 v[24:25], v[0:1], v[24:25], v[26:27] op_sel_hi:[0,1,1]
	s_nop 0
	v_pk_fma_f32 v[18:19], v[18:19], v[30:31], v[28:29]
	v_pk_fma_f32 v[20:21], v[20:21], v[24:25], v[22:23]
	global_store_dwordx4 v[6:7], v[18:21], off offset:-2048
	s_nop 0
	s_nop 0
	s_nop 0
	s_nop 0
	s_nop 0
	s_waitcnt vmcnt(19)
	v_mov_b32_e32 v22, v54
	v_mov_b32_e32 v23, v55
	v_mov_b32_e32 v24, v56
	v_mov_b32_e32 v25, v57
	v_mov_b32_e32 v26, v58
	v_mov_b32_e32 v27, v59
	v_mov_b32_e32 v18, v60
	v_mov_b32_e32 v19, v61
	v_mov_b32_e32 v20, v62
	v_mov_b32_e32 v21, v63
	v_lshlrev_b32_e32 v28, 16, v22
	s_nop 0
	v_lshlrev_b32_e32 v30, 16, v24
	s_nop 0
	v_lshlrev_b32_e32 v32, 16, v26
	v_and_b32_e32 v33, 0xffff0000, v26
	v_lshlrev_b32_e32 v26, 16, v27
	v_and_b32_e32 v27, 0xffff0000, v27
	v_and_b32_e32 v31, 0xffff0000, v24
	v_lshlrev_b32_e32 v24, 16, v25
	v_and_b32_e32 v25, 0xffff0000, v25
	v_pk_mul_f32 v[32:33], v[8:9], v[32:33] op_sel_hi:[0,1]
	v_pk_mul_f32 v[26:27], v[8:9], v[26:27] op_sel_hi:[0,1]
	v_and_b32_e32 v29, 0xffff0000, v22
	v_lshlrev_b32_e32 v22, 16, v23
	v_and_b32_e32 v23, 0xffff0000, v23
	v_pk_fma_f32 v[30:31], v[0:1], v[30:31], v[32:33] op_sel_hi:[0,1,1]
	v_pk_fma_f32 v[24:25], v[0:1], v[24:25], v[26:27] op_sel_hi:[0,1,1]
	s_nop 0
	v_pk_fma_f32 v[18:19], v[18:19], v[30:31], v[28:29]
	v_pk_fma_f32 v[20:21], v[20:21], v[24:25], v[22:23]
	global_store_dwordx4 v[6:7], v[18:21], off offset:-1024
	s_nop 0
	s_nop 0
	s_nop 0
	s_nop 0
	s_nop 0
	s_waitcnt vmcnt(16)
	v_mov_b32_e32 v22, v64
	v_mov_b32_e32 v23, v65
	v_mov_b32_e32 v24, v66
	v_mov_b32_e32 v25, v67
	v_mov_b32_e32 v26, v68
	v_mov_b32_e32 v27, v69
	v_mov_b32_e32 v18, v70
	v_mov_b32_e32 v19, v71
	v_mov_b32_e32 v20, v72
	v_mov_b32_e32 v21, v73
	v_lshlrev_b32_e32 v28, 16, v22
	s_nop 0
	v_lshlrev_b32_e32 v30, 16, v24
	s_nop 0
	v_lshlrev_b32_e32 v32, 16, v26
	v_and_b32_e32 v33, 0xffff0000, v26
	v_lshlrev_b32_e32 v26, 16, v27
	v_and_b32_e32 v27, 0xffff0000, v27
	v_and_b32_e32 v31, 0xffff0000, v24
	v_lshlrev_b32_e32 v24, 16, v25
	v_and_b32_e32 v25, 0xffff0000, v25
	v_pk_mul_f32 v[32:33], v[8:9], v[32:33] op_sel_hi:[0,1]
	v_pk_mul_f32 v[26:27], v[8:9], v[26:27] op_sel_hi:[0,1]
	v_and_b32_e32 v29, 0xffff0000, v22
	v_lshlrev_b32_e32 v22, 16, v23
	v_and_b32_e32 v23, 0xffff0000, v23
	v_pk_fma_f32 v[30:31], v[0:1], v[30:31], v[32:33] op_sel_hi:[0,1,1]
	v_pk_fma_f32 v[24:25], v[0:1], v[24:25], v[26:27] op_sel_hi:[0,1,1]
	s_nop 0
	v_pk_fma_f32 v[18:19], v[18:19], v[30:31], v[28:29]
	v_pk_fma_f32 v[20:21], v[20:21], v[24:25], v[22:23]
	global_store_dwordx4 v[6:7], v[18:21], off
	s_nop 0
	s_nop 0
	s_nop 0
	s_nop 0
	s_nop 0
	s_waitcnt vmcnt(13)
	v_mov_b32_e32 v22, v74
	v_mov_b32_e32 v23, v75
	v_mov_b32_e32 v24, v76
	v_mov_b32_e32 v25, v77
	v_mov_b32_e32 v26, v78
	v_mov_b32_e32 v27, v79
	v_mov_b32_e32 v18, v80
	v_mov_b32_e32 v19, v81
	v_mov_b32_e32 v20, v82
	v_mov_b32_e32 v21, v83
	v_lshlrev_b32_e32 v28, 16, v22
	s_nop 0
	v_lshlrev_b32_e32 v30, 16, v24
	s_nop 0
	v_lshlrev_b32_e32 v32, 16, v26
	v_and_b32_e32 v33, 0xffff0000, v26
	v_lshlrev_b32_e32 v26, 16, v27
	v_and_b32_e32 v27, 0xffff0000, v27
	v_and_b32_e32 v31, 0xffff0000, v24
	v_lshlrev_b32_e32 v24, 16, v25
	v_and_b32_e32 v25, 0xffff0000, v25
	v_pk_mul_f32 v[32:33], v[8:9], v[32:33] op_sel_hi:[0,1]
	v_pk_mul_f32 v[26:27], v[8:9], v[26:27] op_sel_hi:[0,1]
	v_and_b32_e32 v29, 0xffff0000, v22
	v_lshlrev_b32_e32 v22, 16, v23
	v_and_b32_e32 v23, 0xffff0000, v23
	v_pk_fma_f32 v[30:31], v[0:1], v[30:31], v[32:33] op_sel_hi:[0,1,1]
	v_pk_fma_f32 v[24:25], v[0:1], v[24:25], v[26:27] op_sel_hi:[0,1,1]
	s_nop 0
	v_pk_fma_f32 v[18:19], v[18:19], v[30:31], v[28:29]
	v_pk_fma_f32 v[20:21], v[20:21], v[24:25], v[22:23]
	global_store_dwordx4 v[6:7], v[18:21], off offset:1024
	s_nop 0
	s_nop 0
	s_nop 0
	s_nop 0
	s_nop 0
	s_waitcnt vmcnt(10)
	v_mov_b32_e32 v22, v84
	v_mov_b32_e32 v23, v85
	v_mov_b32_e32 v24, v86
	v_mov_b32_e32 v25, v87
	v_mov_b32_e32 v26, v88
	v_mov_b32_e32 v27, v89
	v_mov_b32_e32 v18, v90
	v_mov_b32_e32 v19, v91
	v_mov_b32_e32 v20, v92
	v_mov_b32_e32 v21, v93
	v_lshlrev_b32_e32 v28, 16, v22
	s_nop 0
	v_lshlrev_b32_e32 v30, 16, v24
	s_nop 0
	v_lshlrev_b32_e32 v32, 16, v26
	v_and_b32_e32 v33, 0xffff0000, v26
	v_lshlrev_b32_e32 v26, 16, v27
	v_and_b32_e32 v27, 0xffff0000, v27
	v_and_b32_e32 v31, 0xffff0000, v24
	v_lshlrev_b32_e32 v24, 16, v25
	v_and_b32_e32 v25, 0xffff0000, v25
	v_pk_mul_f32 v[32:33], v[8:9], v[32:33] op_sel_hi:[0,1]
	v_pk_mul_f32 v[26:27], v[8:9], v[26:27] op_sel_hi:[0,1]
	v_and_b32_e32 v29, 0xffff0000, v22
	v_lshlrev_b32_e32 v22, 16, v23
	v_and_b32_e32 v23, 0xffff0000, v23
	v_pk_fma_f32 v[30:31], v[0:1], v[30:31], v[32:33] op_sel_hi:[0,1,1]
	v_pk_fma_f32 v[24:25], v[0:1], v[24:25], v[26:27] op_sel_hi:[0,1,1]
	s_nop 0
	v_pk_fma_f32 v[18:19], v[18:19], v[30:31], v[28:29]
	v_pk_fma_f32 v[20:21], v[20:21], v[24:25], v[22:23]
	global_store_dwordx4 v[6:7], v[18:21], off offset:2048
	s_nop 0
	s_nop 0
	s_nop 0
	s_nop 0
	s_nop 0
	v_lshl_add_u64 v[4:5], v[4:5], 0, s[4:5]
	s_waitcnt vmcnt(7)
	v_mov_b32_e32 v22, v94
	v_mov_b32_e32 v23, v95
	v_mov_b32_e32 v24, v96
	v_mov_b32_e32 v25, v97
	v_mov_b32_e32 v26, v98
	v_mov_b32_e32 v27, v99
	v_mov_b32_e32 v18, v100
	v_mov_b32_e32 v19, v101
	v_mov_b32_e32 v20, v102
	v_mov_b32_e32 v21, v103
	v_lshlrev_b32_e32 v10, 16, v22
	s_nop 0
	v_lshlrev_b32_e32 v12, 16, v24
	s_nop 0
	v_lshlrev_b32_e32 v28, 16, v26
	v_and_b32_e32 v29, 0xffff0000, v26
	v_lshlrev_b32_e32 v26, 16, v27
	v_and_b32_e32 v27, 0xffff0000, v27
	v_and_b32_e32 v13, 0xffff0000, v24
	v_lshlrev_b32_e32 v24, 16, v25
	v_and_b32_e32 v25, 0xffff0000, v25
	v_pk_mul_f32 v[28:29], v[8:9], v[28:29] op_sel_hi:[0,1]
	v_pk_mul_f32 v[26:27], v[8:9], v[26:27] op_sel_hi:[0,1]
	v_and_b32_e32 v11, 0xffff0000, v22
	v_lshlrev_b32_e32 v22, 16, v23
	v_and_b32_e32 v23, 0xffff0000, v23
	v_pk_fma_f32 v[12:13], v[0:1], v[12:13], v[28:29] op_sel_hi:[0,1,1]
	v_pk_fma_f32 v[24:25], v[0:1], v[24:25], v[26:27] op_sel_hi:[0,1,1]
	s_nop 0
	v_pk_fma_f32 v[10:11], v[18:19], v[12:13], v[10:11]
	v_pk_fma_f32 v[12:13], v[20:21], v[24:25], v[22:23]
	global_store_dwordx4 v[6:7], v[10:13], off offset:3072
	v_lshl_add_u64 v[6:7], v[6:7], 0, s[8:9]
	s_cbranch_scc1 .LBB0_2785
